# attention: running row-sum kept per lane, the two half-wave partials combined once after the key loop (one permlane swap per unit instead of per tile)
# speedup vs baseline: 1.0085x; 1.0085x over previous
; __device__ __forceinline__ void partialSM(f32x16& p0, f32x16& p1, float& m_reg, float& alpha, const bool first) {
;     float ma = max3f(p0[0], p0[1], p0[2]), mb = max3f(p0[3], p0[4], p0[5]), mc = max3f(p0[6], p0[7], p0[8]), md = max3f(p0[9], p0[10], p0[11]);
;     ma = max3f(ma, p0[12], p0[13]); mb = max3f(mb, p0[14], p0[15]); mc = max3f(mc, p1[0], p1[1]); md = max3f(md, p1[2], p1[3]);
;     ma = max3f(ma, p1[4], p1[5]); mb = max3f(mb, p1[6], p1[7]); mc = max3f(mc, p1[8], p1[9]); md = max3f(md, p1[10], p1[11]);
;     ma = max3f(ma, p1[12], p1[13]); mb = max3f(mb, p1[14], p1[15]);
;     float pmax = fmaxf(max3f(ma, mb, mc), md);
;     { auto rr = __builtin_amdgcn_permlane32_swap(__float_as_uint(pmax), __float_as_uint(pmax), false, false);
;       pmax = fmaxf(__uint_as_float(rr[0]), __uint_as_float(rr[1])); }
;     const float u = pmax - PSH;
;     if (__builtin_expect(!first && __all(u <= THR2), 1)) { alpha = 1.f; }
;     else { const float dl = first ? u : fmaxf(u, 0.f); alpha = __builtin_amdgcn_exp2f(-dl); m_reg += dl;
; #pragma unroll
;         for (int r = 0; r < 16; ++r) { p0[r] -= dl; p1[r] -= dl; } }
; #pragma unroll
;     for (int r = 0; r < 16; ++r) p0[r] = __builtin_amdgcn_exp2f(p0[r]);
; }
; __device__ __forceinline__ void finishSM(f32x16& p0, f32x16& p1, float alpha, float& l_reg, v8i& pa) {
; #pragma unroll
;     for (int r = 0; r < 16; ++r) p1[r] = __builtin_amdgcn_exp2f(p1[r]);
;     float sa = p0[0] + p0[1], sb = p0[2] + p0[3], sc = p0[4] + p0[5], sd = p0[6] + p0[7];
;     sa += p0[8]; sb += p0[9]; sc += p0[10]; sd += p0[11]; sa += p0[12]; sb += p0[13]; sc += p0[14]; sd += p0[15];
; #pragma unroll
;     for (int r = 0; r < 16; r += 4) { sa += p1[r]; sb += p1[r + 1]; sc += p1[r + 2]; sd += p1[r + 3]; }
;     float ps = (sa + sb) + (sc + sd);
;     { auto rr = __builtin_amdgcn_permlane32_swap(__float_as_uint(ps), __float_as_uint(ps), false, false);
;       ps = __uint_as_float(rr[0]) + __uint_as_float(rr[1]); }
;     l_reg = l_reg * alpha + ps;
; #pragma unroll
;     for (int c = 0; c < 4; ++c) { pa[c] = (int)pk4_fp8(p0[4 * c], p0[4 * c + 1], p0[4 * c + 2], p0[4 * c + 3]);
;         pa[4 + c] = (int)pk4_fp8(p1[4 * c], p1[4 * c + 1], p1[4 * c + 2], p1[4 * c + 3]); }
; }
; __device__ __forceinline__ void qkt(f32x16& p0, f32x16& p1, const float m_reg, const char* Ks, const v8i* q8, int r32, int hi) {
;     { const float ini = PSH - m_reg;
.LBB0_553:
	v_sub_f32_e32 v80, 0x40400000, v180
	v_mov_b32_e32 v81, v80
	v_mov_b64_e32 v[82:83], v[80:81]
	v_mov_b64_e32 v[84:85], v[80:81]
	v_mov_b64_e32 v[86:87], v[80:81]
	v_mov_b64_e32 v[88:89], v[80:81]
	v_mov_b64_e32 v[90:91], v[80:81]
	v_mov_b64_e32 v[92:93], v[80:81]
	v_mov_b64_e32 v[94:95], v[80:81]
	v_exp_f32_e32 v228, v64
	v_exp_f32_e32 v230, v65
	s_waitcnt lgkmcnt(0)
	v_mfma_scale_f32_32x32x64_f8f6f4 v[96:111], v[96:103], v[120:127], v[80:95], v201, v200 op_sel_hi:[0,0,0]
	v_exp_f32_e32 v222, v66
	v_exp_f32_e32 v223, v67
	v_exp_f32_e32 v229, v68
	v_exp_f32_e32 v231, v69
	v_exp_f32_e32 v226, v70
	v_exp_f32_e32 v227, v71
	v_add_f32_e32 v64, v215, v216
	v_add_f32_e32 v65, v190, v192
	v_add_f32_e32 v66, v213, v214
	v_add_f32_e32 v67, v195, v212
	v_exp_f32_e32 v224, v72
	v_exp_f32_e32 v225, v73
	v_exp_f32_e32 v184, v74
	v_exp_f32_e32 v217, v75
	v_add_f32_e32 v64, v194, v64
	v_mfma_scale_f32_32x32x64_f8f6f4 v[80:95], v[136:143], v[120:127], v[80:95], v201, v200 op_sel_hi:[0,0,0]
	ds_read_b128 v[136:139], v164 offset:64
	ds_read_b128 v[140:143], v164 offset:80
	ds_read_b128 v[144:147], v164 offset:6720
	ds_read_b128 v[148:151], v164 offset:6736
	v_add_f32_e32 v65, v211, v65
	v_add_f32_e32 v66, v186, v66
	v_add_f32_e32 v67, v187, v67
	v_exp_f32_e32 v220, v76
	v_exp_f32_e32 v221, v77
	v_exp_f32_e32 v218, v78
	v_exp_f32_e32 v219, v79
	v_add_f32_e32 v64, v191, v64
	v_add_f32_e32 v65, v193, v65
	v_add_f32_e32 v66, v188, v66
	v_add_f32_e32 v67, v189, v67
	v_add_f32_e32 v64, v228, v64
	v_add_f32_e32 v65, v230, v65
	v_add_f32_e32 v66, v222, v66
	s_waitcnt lgkmcnt(0)
	v_mfma_scale_f32_32x32x64_f8f6f4 v[96:111], v[136:143], v[128:135], v[96:111], v201, v200 op_sel_hi:[0,0,0]
	v_add_f32_e32 v67, v223, v67
	v_add_f32_e32 v64, v229, v64
	v_add_f32_e32 v65, v231, v65
	v_add_f32_e32 v66, v226, v66
	v_add_f32_e32 v67, v227, v67
	v_add_f32_e32 v64, v224, v64
	v_add_f32_e32 v65, v225, v65
	v_add_f32_e32 v66, v184, v66
	v_add_f32_e32 v67, v217, v67
	v_add_f32_e32 v64, v220, v64
	v_add_f32_e32 v65, v221, v65
	v_add_f32_e32 v66, v218, v66
	v_add_f32_e32 v67, v219, v67
	v_add_f32_e32 v64, v65, v64
	v_add_f32_e32 v65, v66, v67
	v_mfma_scale_f32_32x32x64_f8f6f4 v[80:95], v[144:151], v[128:135], v[80:95], v201, v200 op_sel_hi:[0,0,0]
	ds_read_b128 v[136:139], v164 offset:128
	ds_read_b128 v[140:143], v164 offset:144
	ds_read_b128 v[144:147], v164 offset:6784
	ds_read_b128 v[148:151], v164 offset:6800
	v_add_f32_e32 v182, v65, v64
	v_cvt_pk_fp8_f32 v232, v215, v216
	v_cvt_pk_fp8_f32 v236, v228, v230
	v_cvt_pk_fp8_f32 v233, v213, v214
	v_cvt_pk_fp8_f32 v237, v229, v231
	v_cvt_pk_fp8_f32 v234, v194, v211
	v_cvt_pk_fp8_f32 v238, v224, v225
	v_cvt_pk_fp8_f32 v235, v191, v193
	v_cvt_pk_fp8_f32 v239, v220, v221
	s_waitcnt lgkmcnt(0)
	v_mfma_scale_f32_32x32x64_f8f6f4 v[96:111], v[136:143], v[112:119], v[96:111], v201, v200 op_sel_hi:[0,0,0]
	v_cvt_pk_fp8_f32 v232, v190, v192 op_sel:[0,0,1]
	v_cvt_pk_fp8_f32 v236, v222, v223 op_sel:[0,0,1]
	v_cvt_pk_fp8_f32 v233, v195, v212 op_sel:[0,0,1]
	v_cvt_pk_fp8_f32 v237, v226, v227 op_sel:[0,0,1]
	v_cvt_pk_fp8_f32 v234, v186, v187 op_sel:[0,0,1]
	v_cvt_pk_fp8_f32 v238, v184, v217 op_sel:[0,0,1]
	v_cvt_pk_fp8_f32 v235, v188, v189 op_sel:[0,0,1]
	v_cvt_pk_fp8_f32 v239, v218, v219 op_sel:[0,0,1]
	v_mfma_scale_f32_32x32x64_f8f6f4 v[80:95], v[144:151], v[112:119], v[80:95], v201, v200 op_sel_hi:[0,0,0]
	s_mul_i32 s15, s10, 0x5c00
	s_add_i32 s11, s15, 0
	v_add_u32_e32 v64, s11, v161
	v_add_u32_e32 v176, v64, v179
	ds_read_b128 v[144:147], v176 offset:13312
	ds_read_b128 v[148:151], v176 offset:13328
	ds_read_b128 v[136:139], v176 offset:15872
	ds_read_b128 v[140:143], v176 offset:15888
	ds_read_b128 v[72:75], v176 offset:18432
	ds_read_b128 v[76:79], v176 offset:18448
	ds_read_b128 v[64:67], v176 offset:20992
	ds_read_b128 v[68:71], v176 offset:21008
	v_max_f32_e32 v164, v96, v97
	v_max3_f32 v165, v99, v100, v101
	v_max3_f32 v164, v164, v98, v108
	v_max3_f32 v165, v165, v110, v111
	v_max3_f32 v166, v102, v103, v104
	v_max3_f32 v167, v105, v106, v107
	s_waitcnt lgkmcnt(0)
	v_mfma_scale_f32_32x32x64_f8f6f4 v[0:15], v[232:239], v[144:151], v[0:15], v201, v201 op_sel_hi:[0,0,0]
	v_max3_f32 v164, v164, v109, v84
	v_max3_f32 v165, v165, v86, v87
	v_max3_f32 v166, v166, v80, v81
	v_max3_f32 v167, v167, v82, v83
	v_max3_f32 v164, v164, v85, v92
	v_max3_f32 v165, v165, v94, v95
	v_max3_f32 v166, v166, v88, v89
	v_max3_f32 v167, v167, v90, v91
	v_mfma_scale_f32_32x32x64_f8f6f4 v[48:63], v[232:239], v[136:143], v[48:63], v201, v201 op_sel_hi:[0,0,0]
	v_max3_f32 v164, v164, v93, v165
	v_max3_f32 v164, v164, v166, v167
	s_mov_b32 s0, 0x410c551d
	v_cmp_ge_f32_e32 vcc, s0, v164
	s_cmp_eq_u64 vcc, exec
	v_mov_b32_e32 v185, 1.0
	s_cbranch_scc0 .LBB0_570

; __device__ __forceinline__ void partialSM(f32x16& p0, f32x16& p1, float& m_reg, float& alpha, const bool first) {
;     float ma = max3f(p0[0], p0[1], p0[2]), mb = max3f(p0[3], p0[4], p0[5]), mc = max3f(p0[6], p0[7], p0[8]), md = max3f(p0[9], p0[10], p0[11]);
;     ma = max3f(ma, p0[12], p0[13]); mb = max3f(mb, p0[14], p0[15]); mc = max3f(mc, p1[0], p1[1]); md = max3f(md, p1[2], p1[3]);
;     ma = max3f(ma, p1[4], p1[5]); mb = max3f(mb, p1[6], p1[7]); mc = max3f(mc, p1[8], p1[9]); md = max3f(md, p1[10], p1[11]);
;     ma = max3f(ma, p1[12], p1[13]); mb = max3f(mb, p1[14], p1[15]);
;     float pmax = fmaxf(max3f(ma, mb, mc), md);
;     { auto rr = __builtin_amdgcn_permlane32_swap(__float_as_uint(pmax), __float_as_uint(pmax), false, false);
;       pmax = fmaxf(__uint_as_float(rr[0]), __uint_as_float(rr[1])); }
;     const float u = pmax - PSH;
;     if (__builtin_expect(!first && __all(u <= THR2), 1)) { alpha = 1.f; }
;     else { const float dl = first ? u : fmaxf(u, 0.f); alpha = __builtin_amdgcn_exp2f(-dl); m_reg += dl;
; #pragma unroll
;         for (int r = 0; r < 16; ++r) { p0[r] -= dl; p1[r] -= dl; } }
; #pragma unroll
;     for (int r = 0; r < 16; ++r) p0[r] = __builtin_amdgcn_exp2f(p0[r]);
; }
; __device__ __forceinline__ void finishSM(f32x16& p0, f32x16& p1, float alpha, float& l_reg, v8i& pa) {
; #pragma unroll
;     for (int r = 0; r < 16; ++r) p1[r] = __builtin_amdgcn_exp2f(p1[r]);
;     float sa = p0[0] + p0[1], sb = p0[2] + p0[3], sc = p0[4] + p0[5], sd = p0[6] + p0[7];
;     sa += p0[8]; sb += p0[9]; sc += p0[10]; sd += p0[11]; sa += p0[12]; sb += p0[13]; sc += p0[14]; sd += p0[15];
; #pragma unroll
;     for (int r = 0; r < 16; r += 4) { sa += p1[r]; sb += p1[r + 1]; sc += p1[r + 2]; sd += p1[r + 3]; }
;     float ps = (sa + sb) + (sc + sd);
;     { auto rr = __builtin_amdgcn_permlane32_swap(__float_as_uint(ps), __float_as_uint(ps), false, false);
;       ps = __uint_as_float(rr[0]) + __uint_as_float(rr[1]); }
;     l_reg = l_reg * alpha + ps;
; #pragma unroll
;     for (int c = 0; c < 4; ++c) { pa[c] = (int)pk4_fp8(p0[4 * c], p0[4 * c + 1], p0[4 * c + 2], p0[4 * c + 3]);
;         pa[4 + c] = (int)pk4_fp8(p1[4 * c], p1[4 * c + 1], p1[4 * c + 2], p1[4 * c + 3]); }
; }
; __device__ __forceinline__ void qkt(f32x16& p0, f32x16& p1, const float m_reg, const char* Ks, const v8i* q8, int r32, int hi) {
;     { const float ini = PSH - m_reg;
.LBB0_563:
	v_sub_f32_e32 v64, 0x40400000, v180
	v_mov_b32_e32 v65, v64
	v_mov_b64_e32 v[66:67], v[64:65]
	v_mov_b64_e32 v[68:69], v[64:65]
	v_mov_b64_e32 v[70:71], v[64:65]
	v_mov_b64_e32 v[72:73], v[64:65]
	v_mov_b64_e32 v[74:75], v[64:65]
	v_mov_b64_e32 v[76:77], v[64:65]
	v_mov_b64_e32 v[78:79], v[64:65]
	v_exp_f32_e32 v231, v80
	v_exp_f32_e32 v233, v81
	s_waitcnt lgkmcnt(0)
	v_mfma_scale_f32_32x32x64_f8f6f4 v[96:111], v[96:103], v[120:127], v[64:79], v201, v200 op_sel_hi:[0,0,0]
	v_exp_f32_e32 v225, v82
	v_exp_f32_e32 v226, v83
	v_exp_f32_e32 v232, v84
	v_exp_f32_e32 v234, v85
	v_exp_f32_e32 v229, v86
	v_exp_f32_e32 v230, v87
	v_add_f32_e32 v80, v216, v215
	v_add_f32_e32 v81, v194, v192
	v_add_f32_e32 v82, v214, v213
	v_add_f32_e32 v83, v212, v211
	v_exp_f32_e32 v227, v88
	v_exp_f32_e32 v228, v89
	v_exp_f32_e32 v219, v90
	v_exp_f32_e32 v220, v91
	v_add_f32_e32 v80, v193, v80
	v_mfma_scale_f32_32x32x64_f8f6f4 v[64:79], v[136:143], v[120:127], v[64:79], v201, v200 op_sel_hi:[0,0,0]
	ds_read_b128 v[136:139], v164 offset:64
	ds_read_b128 v[140:143], v164 offset:80
	ds_read_b128 v[144:147], v164 offset:6720
	ds_read_b128 v[148:151], v164 offset:6736
	v_add_f32_e32 v81, v195, v81
	v_add_f32_e32 v82, v186, v82
	v_add_f32_e32 v83, v187, v83
	v_exp_f32_e32 v223, v92
	v_exp_f32_e32 v224, v93
	v_exp_f32_e32 v221, v94
	v_exp_f32_e32 v222, v95
	v_add_f32_e32 v80, v190, v80
	v_add_f32_e32 v81, v191, v81
	v_add_f32_e32 v82, v188, v82
	v_add_f32_e32 v83, v189, v83
	v_add_f32_e32 v80, v80, v231
	v_add_f32_e32 v81, v81, v233
	v_add_f32_e32 v82, v82, v225
	s_waitcnt lgkmcnt(0)
	v_mfma_scale_f32_32x32x64_f8f6f4 v[96:111], v[136:143], v[128:135], v[96:111], v201, v200 op_sel_hi:[0,0,0]
	v_add_f32_e32 v83, v83, v226
	v_add_f32_e32 v80, v232, v80
	v_add_f32_e32 v81, v234, v81
	v_add_f32_e32 v82, v229, v82
	v_add_f32_e32 v83, v230, v83
	v_add_f32_e32 v80, v227, v80
	v_add_f32_e32 v81, v228, v81
	v_add_f32_e32 v82, v219, v82
	v_add_f32_e32 v83, v220, v83
	v_add_f32_e32 v80, v223, v80
	v_add_f32_e32 v81, v224, v81
	v_add_f32_e32 v82, v221, v82
	v_add_f32_e32 v83, v222, v83
	v_add_f32_e32 v80, v81, v80
	v_add_f32_e32 v81, v82, v83
	v_mfma_scale_f32_32x32x64_f8f6f4 v[64:79], v[144:151], v[128:135], v[64:79], v201, v200 op_sel_hi:[0,0,0]
	ds_read_b128 v[136:139], v164 offset:128
	ds_read_b128 v[140:143], v164 offset:144
	ds_read_b128 v[144:147], v164 offset:6784
	ds_read_b128 v[148:151], v164 offset:6800
	v_add_f32_e32 v217, v81, v80
	v_cvt_pk_fp8_f32 v236, v215, v216
	v_cvt_pk_fp8_f32 v240, v231, v233
	v_cvt_pk_fp8_f32 v237, v213, v214
	v_cvt_pk_fp8_f32 v241, v232, v234
	v_cvt_pk_fp8_f32 v238, v193, v195
	v_cvt_pk_fp8_f32 v242, v227, v228
	v_cvt_pk_fp8_f32 v239, v190, v191
	v_cvt_pk_fp8_f32 v243, v223, v224
	s_waitcnt lgkmcnt(0)
	v_mfma_scale_f32_32x32x64_f8f6f4 v[96:111], v[136:143], v[112:119], v[96:111], v201, v200 op_sel_hi:[0,0,0]
	v_cvt_pk_fp8_f32 v236, v192, v194 op_sel:[0,0,1]
	v_cvt_pk_fp8_f32 v240, v225, v226 op_sel:[0,0,1]
	v_cvt_pk_fp8_f32 v237, v211, v212 op_sel:[0,0,1]
	v_cvt_pk_fp8_f32 v241, v229, v230 op_sel:[0,0,1]
	v_cvt_pk_fp8_f32 v238, v186, v187 op_sel:[0,0,1]
	v_cvt_pk_fp8_f32 v242, v219, v220 op_sel:[0,0,1]
	v_cvt_pk_fp8_f32 v239, v188, v189 op_sel:[0,0,1]
	v_cvt_pk_fp8_f32 v243, v221, v222 op_sel:[0,0,1]
	v_mfma_scale_f32_32x32x64_f8f6f4 v[64:79], v[144:151], v[112:119], v[64:79], v201, v200 op_sel_hi:[0,0,0]
	v_add3_u32 v84, s12, v161, v179
	ds_read_b128 v[144:147], v84 offset:13312
	ds_read_b128 v[148:151], v84 offset:13328
	ds_read_b128 v[136:139], v84 offset:15872
	ds_read_b128 v[140:143], v84 offset:15888
	ds_read_b128 v[88:91], v84 offset:18432
	ds_read_b128 v[92:95], v84 offset:18448
	ds_read_b128 v[80:83], v84 offset:20992
	ds_read_b128 v[84:87], v84 offset:21008
	s_nop 2
	v_max_f32_e32 v164, v96, v97
	v_max3_f32 v165, v99, v100, v101
	v_max3_f32 v164, v164, v98, v108
	v_max3_f32 v165, v165, v110, v111
	v_max3_f32 v166, v102, v103, v104
	v_max3_f32 v167, v105, v106, v107
	s_waitcnt lgkmcnt(0)
	v_mfma_scale_f32_32x32x64_f8f6f4 v[0:15], v[236:243], v[144:151], v[0:15], v201, v201 op_sel_hi:[0,0,0]
	v_max3_f32 v164, v164, v109, v68
	v_max3_f32 v165, v165, v70, v71
	v_max3_f32 v166, v166, v64, v65
	v_max3_f32 v167, v167, v66, v67
	v_max3_f32 v164, v164, v69, v76
	v_max3_f32 v165, v165, v78, v79
	v_max3_f32 v166, v166, v72, v73
	v_max3_f32 v167, v167, v74, v75
	v_mfma_scale_f32_32x32x64_f8f6f4 v[48:63], v[236:243], v[136:143], v[48:63], v201, v201 op_sel_hi:[0,0,0]
	v_max3_f32 v164, v164, v77, v165
	v_max3_f32 v164, v164, v166, v167
	s_mov_b32 s0, 0x410c551d
	v_cmp_ge_f32_e32 vcc, s0, v164
	s_cmp_eq_u64 vcc, exec
	v_mov_b32_e32 v184, 1.0
	s_cbranch_scc0 .LBB0_571

; #define SBAR() __builtin_amdgcn_sched_barrier(0)
; #define WAITBAR() do { asm volatile("s_waitcnt vmcnt(0)" ::: "memory"); __syncthreads(); } while (0)
; #define RESC(a) do { if (__any((a) < 1.f)) { if (hi == 0) al_l[r32] = (a); asm volatile("s_waitcnt lgkmcnt(0)" ::: "memory"); \
;     _Pragma("unroll") for (int d = 0; d < 4; ++d) _Pragma("unroll") for (int r = 0; r < 16; ++r) o[d][r] *= al_l[crow(r, hi)]; } } while (0)
; __device__ __forceinline__ void attn_unit(const bf16_t* Qb, const unsigned char* Kh, const unsigned char* Vh, bf16_t* Ob, int seq, int cbase, int lbase, int t0, const f32x2* atab, char* lds, const int wave_s) {
;     ...
;     for (int j = 1; j + 1 < NT; j += 2) {
;         { const int bn = 3 - bprev - bj; DMA_TILE(j + 1, bn);
;           SBAR(); qkt(pB0, pB1, m_reg, KBUF(bj), qr, r32, hi);
;           finishSM(pA0, pA1, alA, l_reg, pa); SBAR();
;           pv_d0(o, VBASE(bprev), pa, r32, hi); partialSM(pB0, pB1, m_reg, alB, false);
;           RESC(alB); WAITBAR(); bprev = bj; bj = bn; }
;         { const int bn = 3 - bprev - bj; if (j + 2 < NT) DMA_TILE(j + 2, bn);
;           SBAR(); qkt(pA0, pA1, m_reg, KBUF(bj), qr, r32, hi);
;           finishSM(pB0, pB1, alB, l_reg, pa); SBAR();
;           pv_d0(o, VBASE(bprev), pa, r32, hi); partialSM(pA0, pA1, m_reg, alA, false);
;           RESC(alA); WAITBAR(); bprev = bj; bj = bn; }
;     }
.LBB0_568:
	s_waitcnt vmcnt(0)
	s_addk_i32 s7, 0x80
	s_add_i32 s0, s14, 1
	s_addk_i32 s8, 0x80
	v_fma_f32 v80, v181, v175, v182
	s_cmp_ge_i32 s0, s6
	s_mov_b64 s[0:1], 0x5000
	v_fma_f32 v175, v80, v185, v217
	v_lshl_add_u64 v[158:159], v[158:159], 0, s[0:1]
	s_waitcnt vmcnt(0)
	s_barrier
	s_cbranch_scc1 .LBB0_572
	s_mov_b32 s11, s10
	s_mov_b32 s13, s14
	v_mov_b32_e32 v181, v184
	s_branch .LBB0_549

; __device__ __forceinline__ unsigned pk4_fp8(float x0, float x1, float x2, float x3) { int w = 0; w = __builtin_amdgcn_cvt_pk_fp8_f32(x0, x1, w, false); w = __builtin_amdgcn_cvt_pk_fp8_f32(x2, x3, w, true); return (unsigned)w; }
; #define SBAR() __builtin_amdgcn_sched_barrier(0)
; __device__ __forceinline__ int crow(int r, int hi) { return (r & 3) + 8 * (r >> 2) + 4 * hi; }
; #define RESC(a) do { if (__any((a) < 1.f)) { if (hi == 0) al_l[r32] = (a); asm volatile("s_waitcnt lgkmcnt(0)" ::: "memory"); \
;     _Pragma("unroll") for (int d = 0; d < 4; ++d) _Pragma("unroll") for (int r = 0; r < 16; ++r) o[d][r] *= al_l[crow(r, hi)]; } } while (0)
; __device__ __forceinline__ void finishSM(f32x16& p0, f32x16& p1, float alpha, float& l_reg, v8i& pa) {
; #pragma unroll
;     for (int r = 0; r < 16; ++r) p1[r] = __builtin_amdgcn_exp2f(p1[r]);
;     float sa = p0[0] + p0[1], sb = p0[2] + p0[3], sc = p0[4] + p0[5], sd = p0[6] + p0[7];
;     sa += p0[8]; sb += p0[9]; sc += p0[10]; sd += p0[11]; sa += p0[12]; sb += p0[13]; sc += p0[14]; sd += p0[15];
; #pragma unroll
;     for (int r = 0; r < 16; r += 4) { sa += p1[r]; sb += p1[r + 1]; sc += p1[r + 2]; sd += p1[r + 3]; }
;     float ps = (sa + sb) + (sc + sd);
;     { auto rr = __builtin_amdgcn_permlane32_swap(__float_as_uint(ps), __float_as_uint(ps), false, false);
;       ps = __uint_as_float(rr[0]) + __uint_as_float(rr[1]); }
;     l_reg = l_reg * alpha + ps;
; #pragma unroll
;     for (int c = 0; c < 4; ++c) { pa[c] = (int)pk4_fp8(p0[4 * c], p0[4 * c + 1], p0[4 * c + 2], p0[4 * c + 3]);
;         pa[4 + c] = (int)pk4_fp8(p1[4 * c], p1[4 * c + 1], p1[4 * c + 2], p1[4 * c + 3]); }
; __device__ __forceinline__ void attn_unit(const bf16_t* Qb, const unsigned char* Kh, const unsigned char* Vh, bf16_t* Ob, int seq, int cbase, int lbase, int t0, const f32x2* atab, char* lds, const int wave_s) {
;     ...
;     SBAR(); qkt(pB0, pB1, m_reg, KBUF(bj), qr, r32, hi);
;     finishSM(pA0, pA1, alA, l_reg, pa); SBAR();
;     pv_d0(o, VBASE(bprev), pa, r32, hi); partialSM(pB0, pB1, m_reg, alB, false);
;     RESC(alB);
;     finishSM(pB0, pB1, alB, l_reg, pa); SBAR();
;     pv_d0(o, VBASE(bj), pa, r32, hi);
;     if (hi == 0) li_l[r32] = l_reg; asm volatile("s_waitcnt lgkmcnt(0)" ::: "memory");
;     float rli[16];
; #pragma unroll
;     for (int r = 0; r < 16; ++r) rli[r] = 8.f * __builtin_amdgcn_rcpf(li_l[crow(r, hi)]);
.LBB0_577:
	v_exp_f32_e32 v118, v96
	v_exp_f32_e32 v119, v97
	v_exp_f32_e32 v112, v98
	v_exp_f32_e32 v113, v99
	v_exp_f32_e32 v116, v100
	v_exp_f32_e32 v117, v101
	v_exp_f32_e32 v114, v102
	v_exp_f32_e32 v115, v103
	v_exp_f32_e32 v102, v104
	v_exp_f32_e32 v103, v105
	v_exp_f32_e32 v96, v106
	v_exp_f32_e32 v97, v107
	v_exp_f32_e32 v100, v108
	v_exp_f32_e32 v101, v109
	v_exp_f32_e32 v98, v110
	v_exp_f32_e32 v99, v111
	v_exp_f32_e32 v126, v80
	v_exp_f32_e32 v127, v81
	v_exp_f32_e32 v120, v82
	v_exp_f32_e32 v121, v83
	v_exp_f32_e32 v124, v84
	v_exp_f32_e32 v125, v85
	v_exp_f32_e32 v122, v86
	v_exp_f32_e32 v123, v87
	v_add_f32_e32 v64, v119, v118
	v_add_f32_e32 v65, v113, v112
	v_add_f32_e32 v66, v117, v116
	v_add_f32_e32 v67, v115, v114
	v_exp_f32_e32 v110, v88
	v_exp_f32_e32 v111, v89
	v_exp_f32_e32 v104, v90
	v_exp_f32_e32 v105, v91
	v_add_f32_e32 v64, v102, v64
	v_add_f32_e32 v65, v103, v65
	v_add_f32_e32 v66, v96, v66
	v_add_f32_e32 v67, v97, v67
	v_exp_f32_e32 v108, v92
	v_exp_f32_e32 v109, v93
	v_exp_f32_e32 v106, v94
	v_exp_f32_e32 v107, v95
	v_add_f32_e32 v64, v100, v64
	v_add_f32_e32 v65, v101, v65
	v_add_f32_e32 v66, v98, v66
	v_add_f32_e32 v67, v99, v67
	v_add_f32_e32 v64, v126, v64
	v_add_f32_e32 v65, v65, v127
	v_add_f32_e32 v66, v66, v120
	v_add_f32_e32 v67, v67, v121
	v_add_f32_e32 v64, v124, v64
	v_add_f32_e32 v65, v125, v65
	v_add_f32_e32 v66, v122, v66
	v_add_f32_e32 v67, v123, v67
	v_add_f32_e32 v64, v110, v64
	v_add_f32_e32 v65, v111, v65
	v_add_f32_e32 v66, v104, v66
	v_add_f32_e32 v67, v105, v67
	v_add_f32_e32 v64, v108, v64
	v_add_f32_e32 v65, v109, v65
	v_add_f32_e32 v66, v106, v66
	v_add_f32_e32 v67, v107, v67
	v_add_f32_e32 v64, v65, v64
	v_add_f32_e32 v65, v66, v67
	v_add_f32_e32 v131, v65, v64
	v_mov_b32_e32 v132, v131
	s_nop 1
	v_permlane32_swap_b32_e32 v131, v132
	v_mov_b32_e32 v183, v175
	s_nop 1
	v_permlane32_swap_b32_e32 v175, v183
	v_add_f32_e32 v175, v175, v183
	ds_read_b128 v[88:91], v176 offset:13312
	ds_read_b128 v[92:95], v176 offset:13328
	ds_read_b128 v[80:83], v176 offset:15872
	ds_read_b128 v[84:87], v176 offset:15888
	ds_read_b128 v[72:75], v176 offset:18432
	ds_read_b128 v[76:79], v176 offset:18448
	ds_read_b128 v[64:67], v176 offset:20992
	ds_read_b128 v[68:71], v176 offset:21008
	s_and_saveexec_b64 s[0:1], s[44:45]
	v_add_f32_e32 v128, v128, v129
	v_fmac_f32_e32 v128, v175, v184
	v_add_f32_e32 v129, v131, v132
	v_fmac_f32_e32 v129, v128, v130
	ds_write_b32 v174, v129
	s_or_b64 exec, exec, s[0:1]
	v_cvt_pk_fp8_f32 v128, v118, v119
	v_cvt_pk_fp8_f32 v132, v126, v127
	v_cvt_pk_fp8_f32 v129, v116, v117
	v_cvt_pk_fp8_f32 v133, v124, v125
	v_cvt_pk_fp8_f32 v130, v102, v103
	v_cvt_pk_fp8_f32 v134, v110, v111
	v_cvt_pk_fp8_f32 v131, v100, v101
	v_cvt_pk_fp8_f32 v135, v108, v109
	v_cvt_pk_fp8_f32 v128, v112, v113 op_sel:[0,0,1]
	v_cvt_pk_fp8_f32 v132, v120, v121 op_sel:[0,0,1]
	v_cvt_pk_fp8_f32 v129, v114, v115 op_sel:[0,0,1]
	v_cvt_pk_fp8_f32 v133, v122, v123 op_sel:[0,0,1]
	v_cvt_pk_fp8_f32 v130, v96, v97 op_sel:[0,0,1]
	v_cvt_pk_fp8_f32 v134, v104, v105 op_sel:[0,0,1]
	v_cvt_pk_fp8_f32 v131, v98, v99 op_sel:[0,0,1]
	v_cvt_pk_fp8_f32 v135, v106, v107 op_sel:[0,0,1]
	s_waitcnt lgkmcnt(0)
	v_readlane_b32 s0, v255, 18
	v_readlane_b32 s2, v253, 34
	s_waitcnt lgkmcnt(6)
	v_mfma_scale_f32_32x32x64_f8f6f4 v[0:15], v[128:135], v[88:95], v[0:15], v201, v201 op_sel_hi:[0,0,0]
	v_add_u32_e32 v88, s31, v173
	s_lshl_b32 s0, s0, 7
	v_readlane_b32 s3, v253, 35
	s_ashr_i32 s1, s0, 31
	s_lshl_b64 s[6:7], s[2:3], 11
	v_readlane_b32 s2, v248, 53
	v_readlane_b32 s3, v248, 54
	s_add_u32 s2, s2, s6
	s_addc_u32 s3, s3, s7
	s_lshl_b64 s[0:1], s[0:1], 1
	s_add_u32 s0, s2, s0
	s_addc_u32 s1, s3, s1
	v_readlane_b32 s2, v248, 32
	v_readlane_b32 s3, v248, 33
	s_add_u32 s0, s0, s2
	s_waitcnt lgkmcnt(4)
	v_mfma_scale_f32_32x32x64_f8f6f4 v[48:63], v[128:135], v[80:87], v[48:63], v201, v201 op_sel_hi:[0,0,0]
	ds_read_b128 v[80:83], v88
	ds_read_b128 v[84:87], v88 offset:32
	s_addc_u32 s1, s1, s3
	v_lshlrev_b32_e32 v152, 1, v155
	s_waitcnt lgkmcnt(1)
	v_rcp_f32_e32 v80, v80
	v_rcp_f32_e32 v81, v81
	v_rcp_f32_e32 v82, v82
	v_rcp_f32_e32 v83, v83
	v_mul_f32_e32 v80, 0x41000000, v80
	v_mul_f32_e32 v0, v0, v80
	v_cvt_pk_bf16_f32 v0, v0, v153
	v_mul_f32_e32 v81, 0x41000000, v81
	v_mul_f32_e32 v82, 0x41000000, v82
	v_mul_f32_e32 v83, 0x41000000, v83
	v_mfma_scale_f32_32x32x64_f8f6f4 v[32:47], v[128:135], v[72:79], v[32:47], v201, v201 op_sel_hi:[0,0,0]
	ds_read_b128 v[72:75], v88 offset:64
	ds_read_b128 v[76:79], v88 offset:96
	s_waitcnt lgkmcnt(2)
	v_rcp_f32_e32 v84, v84
	v_rcp_f32_e32 v85, v85
	v_rcp_f32_e32 v86, v86
	s_waitcnt lgkmcnt(1)
	v_rcp_f32_e32 v73, v73
	v_rcp_f32_e32 v74, v74
	v_rcp_f32_e32 v75, v75
	v_mul_f32_e32 v84, 0x41000000, v84
	v_mul_f32_e32 v85, 0x41000000, v85
	v_mul_f32_e32 v86, 0x41000000, v86
	v_rcp_f32_e32 v87, v87
	v_rcp_f32_e32 v72, v72
	v_mul_f32_e32 v87, 0x41000000, v87
	v_mfma_scale_f32_32x32x64_f8f6f4 v[16:31], v[128:135], v[64:71], v[16:31], v201, v201 op_sel_hi:[0,0,0]
	s_waitcnt lgkmcnt(0)
; __device__ __forceinline__ unsigned f2bf(float f) { return pk2(f, 0.f) & 0xffffu; }
; __device__ __forceinline__ int crow(int r, int hi) { return (r & 3) + 8 * (r >> 2) + 4 * hi; }
; __device__ __forceinline__ void attn_unit(const bf16_t* Qb, const unsigned char* Kh, const unsigned char* Vh, bf16_t* Ob, int seq, int cbase, int lbase, int t0, const f32x2* atab, char* lds, const int wave_s) {
;     ...
;     if (hi == 0) li_l[r32] = l_reg; asm volatile("s_waitcnt lgkmcnt(0)" ::: "memory");
;     float rli[16];
; #pragma unroll
;     for (int r = 0; r < 16; ++r) rli[r] = 8.f * __builtin_amdgcn_rcpf(li_l[crow(r, hi)]);
;     bf16_t* Ow = Ob + (long)(wid * QBLK) * LDO;
; #pragma unroll
;     for (int r = 0; r < 16; ++r) { const int orow = crow(r, hi);
; #pragma unroll
;         for (int d0 = 0; d0 < 4; ++d0) Ow[(long)orow * LDO + d0 * 32 + r32] = (bf16_t)f2bf(o[d0][r] * rli[r]); }
	v_rcp_f32_e32 v64, v76
	v_rcp_f32_e32 v65, v77
	v_rcp_f32_e32 v66, v78
	v_rcp_f32_e32 v67, v79
	v_mul_f32_e32 v68, 0x41000000, v73
	v_mul_f32_e32 v69, 0x41000000, v74
	v_mul_f32_e32 v70, 0x41000000, v75
	v_mul_f32_e32 v71, 0x41000000, v64
	v_mul_f32_e32 v73, 0x41000000, v65
	v_mul_f32_e32 v74, 0x41000000, v66
	v_mul_f32_e32 v75, 0x41000000, v67
	v_lshlrev_b32_e32 v64, 13, v172
	v_lshl_add_u64 v[66:67], s[0:1], 0, v[152:153]
	v_mov_b32_e32 v65, v153
	v_lshl_add_u64 v[64:65], v[66:67], 0, v[64:65]
	global_store_short v[64:65], v0, off
	v_mul_f32_e32 v0, v48, v80
	v_cvt_pk_bf16_f32 v0, v0, v153
	global_store_short v[64:65], v0, off offset:64
	v_mul_f32_e32 v0, v32, v80
	v_cvt_pk_bf16_f32 v0, v0, v153
	global_store_short v[64:65], v0, off offset:128
	v_mul_f32_e32 v0, v16, v80
	v_cvt_pk_bf16_f32 v0, v0, v153
	global_store_short v[64:65], v0, off offset:192
	v_mul_f32_e32 v0, v1, v81
	v_cvt_pk_bf16_f32 v0, v0, v153
	global_store_short v[64:65], v0, off offset:2048
	v_mul_f32_e32 v0, v49, v81
	v_cvt_pk_bf16_f32 v0, v0, v153
	global_store_short v[64:65], v0, off offset:2112
	v_mul_f32_e32 v0, v33, v81
	v_cvt_pk_bf16_f32 v0, v0, v153
	global_store_short v[64:65], v0, off offset:2176
	v_mul_f32_e32 v0, v17, v81
	v_cvt_pk_bf16_f32 v0, v0, v153
	global_store_short v[64:65], v0, off offset:2240
	v_mul_f32_e32 v0, v2, v82
	s_movk_i32 s0, 0x1000
	v_cvt_pk_bf16_f32 v2, v0, v153
	v_add_co_u32_e32 v0, vcc, s0, v64
	s_movk_i32 s0, 0x4000
	s_nop 0
	v_addc_co_u32_e32 v1, vcc, 0, v65, vcc
	global_store_short v[0:1], v2, off
	v_mul_f32_e32 v2, v50, v82
	v_cvt_pk_bf16_f32 v2, v2, v153
	global_store_short v[0:1], v2, off offset:64
	v_mul_f32_e32 v2, v34, v82
	v_cvt_pk_bf16_f32 v2, v2, v153
	global_store_short v[0:1], v2, off offset:128
	v_mul_f32_e32 v2, v18, v82
	v_cvt_pk_bf16_f32 v2, v2, v153
	global_store_short v[0:1], v2, off offset:192
	v_mul_f32_e32 v2, v3, v83
	v_cvt_pk_bf16_f32 v2, v2, v153
	global_store_short v[0:1], v2, off offset:2048
	v_mul_f32_e32 v2, v51, v83
	v_cvt_pk_bf16_f32 v2, v2, v153
	global_store_short v[0:1], v2, off offset:2112
	v_mul_f32_e32 v2, v35, v83
	v_cvt_pk_bf16_f32 v2, v2, v153
	global_store_short v[0:1], v2, off offset:2176
	v_mul_f32_e32 v2, v19, v83
	v_cvt_pk_bf16_f32 v2, v2, v153
	global_store_short v[0:1], v2, off offset:2240
	v_mul_f32_e32 v0, v4, v84
	v_cvt_pk_bf16_f32 v4, v0, v153
	v_add_co_u32_e32 v0, vcc, s0, v64
	s_movk_i32 s0, 0x5000
	s_nop 0
	v_addc_co_u32_e32 v1, vcc, 0, v65, vcc
	v_add_co_u32_e32 v2, vcc, s0, v64
	v_mul_f32_e32 v72, 0x41000000, v72
	s_nop 0
	v_addc_co_u32_e32 v3, vcc, 0, v65, vcc
	global_store_short v[2:3], v4, off offset:-4096
	v_mul_f32_e32 v4, v52, v84
	v_cvt_pk_bf16_f32 v4, v4, v153
	global_store_short v[0:1], v4, off offset:64
	v_mul_f32_e32 v4, v36, v84
	v_cvt_pk_bf16_f32 v4, v4, v153
	global_store_short v[0:1], v4, off offset:128
	v_mul_f32_e32 v4, v20, v84
	v_cvt_pk_bf16_f32 v4, v4, v153
	global_store_short v[0:1], v4, off offset:192
	v_mul_f32_e32 v4, v5, v85
	v_cvt_pk_bf16_f32 v4, v4, v153
	global_store_short v[0:1], v4, off offset:2048
	v_mul_f32_e32 v4, v53, v85
	v_cvt_pk_bf16_f32 v4, v4, v153
	global_store_short v[0:1], v4, off offset:2112
	v_mul_f32_e32 v4, v37, v85
	v_cvt_pk_bf16_f32 v4, v4, v153
	global_store_short v[0:1], v4, off offset:2176
	v_mul_f32_e32 v4, v21, v85
	v_cvt_pk_bf16_f32 v4, v4, v153
	global_store_short v[0:1], v4, off offset:2240
	v_mul_f32_e32 v0, v6, v86
	v_cvt_pk_bf16_f32 v0, v0, v153
	global_store_short v[2:3], v0, off
	v_mul_f32_e32 v0, v54, v86
	v_cvt_pk_bf16_f32 v0, v0, v153
	global_store_short v[2:3], v0, off offset:64
	v_mul_f32_e32 v0, v38, v86
	v_cvt_pk_bf16_f32 v0, v0, v153
	global_store_short v[2:3], v0, off offset:128
	v_mul_f32_e32 v0, v22, v86
	v_cvt_pk_bf16_f32 v0, v0, v153
	global_store_short v[2:3], v0, off offset:192
	v_mul_f32_e32 v0, v7, v87
	v_cvt_pk_bf16_f32 v0, v0, v153
	global_store_short v[2:3], v0, off offset:2048
	v_mul_f32_e32 v0, v55, v87
	v_cvt_pk_bf16_f32 v0, v0, v153
	global_store_short v[2:3], v0, off offset:2112
	v_mul_f32_e32 v0, v39, v87
	v_cvt_pk_bf16_f32 v0, v0, v153
	global_store_short v[2:3], v0, off offset:2176
	v_mul_f32_e32 v0, v23, v87
	v_cvt_pk_bf16_f32 v0, v0, v153
	global_store_short v[2:3], v0, off offset:2240
	v_mul_f32_e32 v0, v8, v72
	s_mov_b32 s0, 0x8000
	v_cvt_pk_bf16_f32 v4, v0, v153
; __device__ __forceinline__ unsigned f2bf(float f) { return pk2(f, 0.f) & 0xffffu; }
; __device__ __forceinline__ int crow(int r, int hi) { return (r & 3) + 8 * (r >> 2) + 4 * hi; }
; __device__ __forceinline__ void attn_unit(const bf16_t* Qb, const unsigned char* Kh, const unsigned char* Vh, bf16_t* Ob, int seq, int cbase, int lbase, int t0, const f32x2* atab, char* lds, const int wave_s) {
;     ...
;     for (int r = 0; r < 16; ++r) { const int orow = crow(r, hi);
; #pragma unroll
;         for (int d0 = 0; d0 < 4; ++d0) Ow[(long)orow * LDO + d0 * 32 + r32] = (bf16_t)f2bf(o[d0][r] * rli[r]); }
;     __syncthreads();
	v_add_co_u32_e32 v0, vcc, s0, v64
	s_mov_b32 s0, 0x9000
	s_nop 0
	v_addc_co_u32_e32 v1, vcc, 0, v65, vcc
	v_add_co_u32_e32 v2, vcc, s0, v64
	s_mov_b32 s0, 0xc000
	s_nop 0
	v_addc_co_u32_e32 v3, vcc, 0, v65, vcc
	global_store_short v[2:3], v4, off offset:-4096
	v_mul_f32_e32 v4, v56, v72
	v_cvt_pk_bf16_f32 v4, v4, v153
	global_store_short v[0:1], v4, off offset:64
	v_mul_f32_e32 v4, v40, v72
	v_cvt_pk_bf16_f32 v4, v4, v153
	global_store_short v[0:1], v4, off offset:128
	v_mul_f32_e32 v4, v24, v72
	v_cvt_pk_bf16_f32 v4, v4, v153
	global_store_short v[0:1], v4, off offset:192
	v_mul_f32_e32 v4, v9, v68
	v_cvt_pk_bf16_f32 v4, v4, v153
	global_store_short v[0:1], v4, off offset:2048
	v_mul_f32_e32 v4, v57, v68
	v_cvt_pk_bf16_f32 v4, v4, v153
	global_store_short v[0:1], v4, off offset:2112
	v_mul_f32_e32 v4, v41, v68
	v_cvt_pk_bf16_f32 v4, v4, v153
	global_store_short v[0:1], v4, off offset:2176
	v_mul_f32_e32 v4, v25, v68
	v_cvt_pk_bf16_f32 v4, v4, v153
	global_store_short v[0:1], v4, off offset:2240
	v_mul_f32_e32 v0, v10, v69
	v_cvt_pk_bf16_f32 v0, v0, v153
	global_store_short v[2:3], v0, off
	v_mul_f32_e32 v0, v58, v69
	v_cvt_pk_bf16_f32 v0, v0, v153
	global_store_short v[2:3], v0, off offset:64
	v_mul_f32_e32 v0, v42, v69
	v_cvt_pk_bf16_f32 v0, v0, v153
	global_store_short v[2:3], v0, off offset:128
	v_mul_f32_e32 v0, v26, v69
	v_cvt_pk_bf16_f32 v0, v0, v153
	global_store_short v[2:3], v0, off offset:192
	v_mul_f32_e32 v0, v11, v70
	v_cvt_pk_bf16_f32 v0, v0, v153
	global_store_short v[2:3], v0, off offset:2048
	v_mul_f32_e32 v0, v59, v70
	v_cvt_pk_bf16_f32 v0, v0, v153
	global_store_short v[2:3], v0, off offset:2112
	v_mul_f32_e32 v0, v43, v70
	v_cvt_pk_bf16_f32 v0, v0, v153
	global_store_short v[2:3], v0, off offset:2176
	v_mul_f32_e32 v0, v27, v70
	v_cvt_pk_bf16_f32 v0, v0, v153
	global_store_short v[2:3], v0, off offset:2240
	v_mul_f32_e32 v0, v12, v71
	v_cvt_pk_bf16_f32 v4, v0, v153
	v_add_co_u32_e32 v0, vcc, s0, v64
	s_mov_b32 s0, 0xd000
	s_nop 0
	v_addc_co_u32_e32 v1, vcc, 0, v65, vcc
	v_add_co_u32_e32 v2, vcc, s0, v64
	s_nop 1
	v_addc_co_u32_e32 v3, vcc, 0, v65, vcc
	global_store_short v[2:3], v4, off offset:-4096
	v_mul_f32_e32 v4, v60, v71
	v_cvt_pk_bf16_f32 v4, v4, v153
	global_store_short v[0:1], v4, off offset:64
	v_mul_f32_e32 v4, v44, v71
	v_cvt_pk_bf16_f32 v4, v4, v153
	global_store_short v[0:1], v4, off offset:128
	v_mul_f32_e32 v4, v28, v71
	v_cvt_pk_bf16_f32 v4, v4, v153
	global_store_short v[0:1], v4, off offset:192
	v_mul_f32_e32 v4, v13, v73
	v_cvt_pk_bf16_f32 v4, v4, v153
	global_store_short v[0:1], v4, off offset:2048
	v_mul_f32_e32 v4, v61, v73
	v_cvt_pk_bf16_f32 v4, v4, v153
	global_store_short v[0:1], v4, off offset:2112
	v_mul_f32_e32 v4, v45, v73
	v_cvt_pk_bf16_f32 v4, v4, v153
	global_store_short v[0:1], v4, off offset:2176
	v_mul_f32_e32 v4, v29, v73
	v_cvt_pk_bf16_f32 v4, v4, v153
	global_store_short v[0:1], v4, off offset:2240
	v_mul_f32_e32 v0, v14, v74
	v_cvt_pk_bf16_f32 v0, v0, v153
	global_store_short v[2:3], v0, off
	v_mul_f32_e32 v0, v62, v74
	v_cvt_pk_bf16_f32 v0, v0, v153
	global_store_short v[2:3], v0, off offset:64
	v_mul_f32_e32 v0, v46, v74
	v_cvt_pk_bf16_f32 v0, v0, v153
	global_store_short v[2:3], v0, off offset:128
	v_mul_f32_e32 v0, v30, v74
	v_cvt_pk_bf16_f32 v0, v0, v153
	global_store_short v[2:3], v0, off offset:192
	v_mul_f32_e32 v0, v15, v75
	v_cvt_pk_bf16_f32 v0, v0, v153
	global_store_short v[2:3], v0, off offset:2048
	v_mul_f32_e32 v0, v63, v75
	v_cvt_pk_bf16_f32 v0, v0, v153
	global_store_short v[2:3], v0, off offset:2112
	v_mul_f32_e32 v0, v47, v75
	v_cvt_pk_bf16_f32 v0, v0, v153
	global_store_short v[2:3], v0, off offset:2176
	v_mul_f32_e32 v0, v31, v75
	s_andn2_b64 vcc, exec, s[52:53]
	v_cvt_pk_bf16_f32 v0, v0, v153
	global_store_short v[2:3], v0, off offset:2240
	s_waitcnt vmcnt(63) expcnt(7) lgkmcnt(15)
	s_barrier
	s_cbranch_vccnz .LBB0_583
	s_waitcnt vmcnt(0)
	s_barrier
	s_and_saveexec_b64 s[0:1], s[40:41]
	s_cbranch_execz .LBB0_582
	v_readlane_b32 s2, v255, 17
	s_lshl_b32 s2, s2, 6
	s_add_i32 s6, s2, s62
	s_ashr_i32 s7, s6, 31
	s_lshl_b64 s[6:7], s[6:7], 2
	v_readlane_b32 s2, v248, 34
	s_add_u32 s6, s2, s6
	v_readlane_b32 s2, v248, 35
	s_addc_u32 s7, s2, s7
	buffer_wbl2 sc1
	s_waitcnt vmcnt(0)
	s_waitcnt vmcnt(0)
	global_atomic_add v153, v197, s[6:7]
